# speedup vs baseline: 1.0046x; 1.0046x over previous
.LBB0_23:
	s_andn2_b64 vcc, exec, s[4:5]
	s_cbranch_vccnz .LBB0_43
	s_load_dwordx2 s[4:5], s[0:1], 0x0
	v_readfirstlane_b32 s82, v0
	s_nop 0
	s_bitcmp1_b32 s82, 8
	s_cbranch_scc0 .Lmy_priof_done
	s_setprio 1
.Lmy_priof_done:
	s_add_i32 s3, s2, 0xfffffdd6
	s_ashr_i32 s76, s3, 4
	v_lshlrev_b32_e32 v43, 3, v31
	v_lshl_or_b32 v2, s76, 5, v43
	v_lshrrev_b32_e32 v42, 8, v0
	s_lshl_b32 s3, s3, 1
	v_ashrrev_i32_e32 v3, 31, v2
	v_and_or_b32 v1, s3, 30, v42
	v_lshlrev_b64 v[2:3], 15, v[2:3]
	s_waitcnt lgkmcnt(0)
	v_lshl_add_u64 v[2:3], s[4:5], 0, v[2:3]
	v_lshlrev_b32_e32 v38, 10, v1
	v_mov_b32_e32 v39, 0
	v_lshl_add_u64 v[2:3], v[2:3], 0, v[38:39]
	v_lshlrev_b32_e32 v38, 4, v30
	v_lshl_add_u64 v[2:3], v[2:3], 0, v[38:39]
	s_mov_b32 s3, 0x8000
	v_add_co_u32_e32 v4, vcc, s3, v2
	s_mov_b32 s3, 0x10000
	s_nop 0
	v_addc_co_u32_e32 v5, vcc, 0, v3, vcc
	global_load_dwordx4 v[34:37], v[2:3], off nt
	global_load_dwordx4 v[26:29], v[4:5], off nt
	v_add_co_u32_e32 v4, vcc, s3, v2
	s_mov_b32 s3, 0x18000
	s_nop 0
	v_addc_co_u32_e32 v5, vcc, 0, v3, vcc
	v_add_co_u32_e32 v6, vcc, s3, v2
	s_mov_b32 s3, 0x20000
	s_nop 0
	v_addc_co_u32_e32 v7, vcc, 0, v3, vcc
	global_load_dwordx4 v[22:25], v[4:5], off nt
	global_load_dwordx4 v[18:21], v[6:7], off nt
	v_add_co_u32_e32 v4, vcc, s3, v2
	s_mov_b32 s3, 0x28000
	s_nop 0
	v_addc_co_u32_e32 v5, vcc, 0, v3, vcc
	v_add_co_u32_e32 v6, vcc, s3, v2
	s_mov_b32 s3, 0x30000
	s_nop 0
	v_addc_co_u32_e32 v7, vcc, 0, v3, vcc
	v_add_co_u32_e32 v32, vcc, s3, v2
	s_mov_b32 s3, 0x38000
	s_nop 0
	v_addc_co_u32_e32 v33, vcc, 0, v3, vcc
	v_add_co_u32_e32 v40, vcc, s3, v2
	global_load_dwordx4 v[14:17], v[4:5], off nt
	global_load_dwordx4 v[10:13], v[6:7], off nt
	v_addc_co_u32_e32 v41, vcc, 0, v3, vcc
	global_load_dwordx4 v[6:9], v[32:33], off nt
	global_load_dwordx4 v[2:5], v[40:41], off nt
	v_mbcnt_lo_u32_b32 v33, -1, 0
	v_mbcnt_hi_u32_b32 v33, -1, v33
	v_and_b32_e32 v40, 64, v33
	v_xor_b32_e32 v39, 1, v33
	v_add_u32_e32 v40, 64, v40
	v_cmp_lt_i32_e32 vcc, v39, v40
	v_mov_b32_e32 v32, 0x800
	v_lshl_or_b32 v32, v42, 10, v32
	v_cndmask_b32_e32 v33, v33, v39, vcc
	v_lshlrev_b32_e32 v33, 2, v33
	s_waitcnt vmcnt(7)
	v_cmp_neq_f32_e32 vcc, 0, v34
	s_nop 1
	v_cndmask_b32_e64 v34, 0, 1, vcc
	v_cmp_neq_f32_e32 vcc, 0, v35
	s_nop 1
	v_cndmask_b32_e64 v35, 0, 2, vcc
	v_cmp_neq_f32_e32 vcc, 0, v36
	v_or_b32_e32 v34, v35, v34
	s_nop 0
	v_cndmask_b32_e64 v36, 0, 4, vcc
	v_cmp_neq_f32_e32 vcc, 0, v37
	s_nop 1
	v_cndmask_b32_e64 v35, 0, 8, vcc
	v_or3_b32 v35, v34, v36, v35
	ds_bpermute_b32 v36, v33, v35
	v_and_b32_e32 v34, 1, v0
	v_cmp_eq_u32_e32 vcc, 0, v34
	v_or_b32_e32 v34, v32, v43
	v_add_u32_e32 v34, v34, v38
	s_and_saveexec_b64 s[4:5], vcc
	s_cbranch_execz .LBB0_26
	s_waitcnt lgkmcnt(0)
	v_lshl_or_b32 v35, v36, 4, v35
	ds_write_b8 v34, v35

	.amdhsa_kernel _Z7k_frontPKfPmS0_S0_S0_S0_S0_S0_PDF16_S2_PfS3_S0_S2_S0_S2_S3_S3_S3_
		.amdhsa_group_segment_fixed_size 4096
		.amdhsa_private_segment_fixed_size 0
		.amdhsa_kernarg_size 152
		.amdhsa_user_sgpr_count 2
		.amdhsa_user_sgpr_dispatch_ptr 0
		.amdhsa_user_sgpr_queue_ptr 0
		.amdhsa_user_sgpr_kernarg_segment_ptr 1
		.amdhsa_user_sgpr_dispatch_id 0
		.amdhsa_user_sgpr_kernarg_preload_length 0
		.amdhsa_user_sgpr_kernarg_preload_offset 0
		.amdhsa_user_sgpr_private_segment_size 0
		.amdhsa_uses_dynamic_stack 0
		.amdhsa_enable_private_segment 0
		.amdhsa_system_sgpr_workgroup_id_x 1
		.amdhsa_system_sgpr_workgroup_id_y 0
		.amdhsa_system_sgpr_workgroup_id_z 0
		.amdhsa_system_sgpr_workgroup_info 0
		.amdhsa_system_vgpr_workitem_id 0
		.amdhsa_next_free_vgpr 68
		.amdhsa_next_free_sgpr 83
		.amdhsa_accum_offset 68
		.amdhsa_reserve_vcc 1
		.amdhsa_float_round_mode_32 0
		.amdhsa_float_round_mode_16_64 0
		.amdhsa_float_denorm_mode_32 3
		.amdhsa_float_denorm_mode_16_64 3
		.amdhsa_dx10_clamp 1
		.amdhsa_ieee_mode 1
		.amdhsa_fp16_overflow 0
		.amdhsa_tg_split 0
		.amdhsa_exception_fp_ieee_invalid_op 0
		.amdhsa_exception_fp_denorm_src 0
		.amdhsa_exception_fp_ieee_div_zero 0
		.amdhsa_exception_fp_ieee_overflow 0
		.amdhsa_exception_fp_ieee_underflow 0
		.amdhsa_exception_fp_ieee_inexact 0
		.amdhsa_exception_int_div_zero 0
	.end_amdhsa_kernel

amdhsa.kernels:
  - .agpr_count:     0
    .args:
      - .actual_access:  read_only
        .address_space:  global
        .offset:         0
        .size:           8
        .value_kind:     global_buffer
      - .address_space:  global
        .offset:         8
        .size:           8
        .value_kind:     global_buffer
      - .actual_access:  read_only
        .address_space:  global
        .offset:         16
        .size:           8
        .value_kind:     global_buffer
      - .actual_access:  read_only
        .address_space:  global
        .offset:         24
        .size:           8
        .value_kind:     global_buffer
      - .actual_access:  read_only
        .address_space:  global
        .offset:         32
        .size:           8
        .value_kind:     global_buffer
      - .actual_access:  read_only
        .address_space:  global
        .offset:         40
        .size:           8
        .value_kind:     global_buffer
      - .actual_access:  read_only
        .address_space:  global
        .offset:         48
        .size:           8
        .value_kind:     global_buffer
      - .actual_access:  read_only
        .address_space:  global
        .offset:         56
        .size:           8
        .value_kind:     global_buffer
      - .actual_access:  write_only
        .address_space:  global
        .offset:         64
        .size:           8
        .value_kind:     global_buffer
      - .actual_access:  write_only
        .address_space:  global
        .offset:         72
        .size:           8
        .value_kind:     global_buffer
      - .actual_access:  write_only
        .address_space:  global
        .offset:         80
        .size:           8
        .value_kind:     global_buffer
      - .actual_access:  write_only
        .address_space:  global
        .offset:         88
        .size:           8
        .value_kind:     global_buffer
      - .actual_access:  read_only
        .address_space:  global
        .offset:         96
        .size:           8
        .value_kind:     global_buffer
      - .actual_access:  write_only
        .address_space:  global
        .offset:         104
        .size:           8
        .value_kind:     global_buffer
      - .actual_access:  read_only
        .address_space:  global
        .offset:         112
        .size:           8
        .value_kind:     global_buffer
      - .actual_access:  write_only
        .address_space:  global
        .offset:         120
        .size:           8
        .value_kind:     global_buffer
      - .actual_access:  write_only
        .address_space:  global
        .offset:         128
        .size:           8
        .value_kind:     global_buffer
      - .actual_access:  write_only
        .address_space:  global
        .offset:         136
        .size:           8
        .value_kind:     global_buffer
      - .actual_access:  write_only
        .address_space:  global
        .offset:         144
        .size:           8
        .value_kind:     global_buffer
    .group_segment_fixed_size: 4096
    .kernarg_segment_align: 8
    .kernarg_segment_size: 152
    .language:       OpenCL C
    .language_version:
      - 2
      - 0
    .max_flat_workgroup_size: 512
    .name:           _Z7k_frontPKfPmS0_S0_S0_S0_S0_S0_PDF16_S2_PfS3_S0_S2_S0_S2_S3_S3_S3_
    .private_segment_fixed_size: 0
    .sgpr_count:     89
    .sgpr_spill_count: 0
    .symbol:         _Z7k_frontPKfPmS0_S0_S0_S0_S0_S0_PDF16_S2_PfS3_S0_S2_S0_S2_S3_S3_S3_.kd
    .uniform_work_group_size: 1
    .uses_dynamic_stack: false
    .vgpr_count:     68
    .vgpr_spill_count: 0
    .wavefront_size: 64
  - .agpr_count:     256
    .args:
      - .actual_access:  read_only
        .address_space:  global
        .offset:         0
        .size:           8
        .value_kind:     global_buffer
      - .actual_access:  read_only
        .address_space:  global
        .offset:         8
        .size:           8
        .value_kind:     global_buffer
      - .actual_access:  read_only
        .address_space:  global
        .offset:         16
        .size:           8
        .value_kind:     global_buffer
      - .actual_access:  read_only
        .address_space:  global
        .offset:         24
        .size:           8
        .value_kind:     global_buffer
      - .actual_access:  read_only
        .address_space:  global
        .offset:         32
        .size:           8
        .value_kind:     global_buffer
      - .address_space:  global
        .offset:         40
        .size:           8
        .value_kind:     global_buffer
      - .actual_access:  write_only
        .address_space:  global
        .offset:         48
        .size:           8
        .value_kind:     global_buffer
      - .actual_access:  write_only
        .address_space:  global
        .offset:         56
        .size:           8
        .value_kind:     global_buffer
    .group_segment_fixed_size: 114688
    .kernarg_segment_align: 8
    .kernarg_segment_size: 64
    .language:       OpenCL C
    .language_version:
      - 2
      - 0
    .max_flat_workgroup_size: 256
    .name:           _Z6k_mainPKDF16_PKfS2_S2_PKmPjPfS6_
    .private_segment_fixed_size: 0
    .sgpr_count:     108
    .sgpr_spill_count: 0
    .symbol:         _Z6k_mainPKDF16_PKfS2_S2_PKmPjPfS6_.kd
    .uniform_work_group_size: 1
    .uses_dynamic_stack: false
    .vgpr_count:     492
    .vgpr_spill_count: 0
    .wavefront_size: 64
  - .agpr_count:     0
    .args:
      - .actual_access:  read_only
        .address_space:  global
        .offset:         0
        .size:           8
        .value_kind:     global_buffer
      - .actual_access:  read_only
        .address_space:  global
        .offset:         8
        .size:           8
        .value_kind:     global_buffer
      - .actual_access:  read_only
        .address_space:  global
        .offset:         16
        .size:           8
        .value_kind:     global_buffer
      - .actual_access:  read_only
        .address_space:  global
        .offset:         24
        .size:           8
        .value_kind:     global_buffer
      - .actual_access:  read_only
        .address_space:  global
        .offset:         32
        .size:           8
        .value_kind:     global_buffer
      - .actual_access:  read_only
        .address_space:  global
        .offset:         40
        .size:           8
        .value_kind:     global_buffer
      - .actual_access:  read_only
        .address_space:  global
        .offset:         48
        .size:           8
        .value_kind:     global_buffer
      - .actual_access:  read_only
        .address_space:  global
        .offset:         56
        .size:           8
        .value_kind:     global_buffer
      - .actual_access:  read_only
        .address_space:  global
        .offset:         64
        .size:           8
        .value_kind:     global_buffer
      - .actual_access:  write_only
        .address_space:  global
        .offset:         72
        .size:           8
        .value_kind:     global_buffer
      - .actual_access:  write_only
        .address_space:  global
        .offset:         80
        .size:           8
        .value_kind:     global_buffer
    .group_segment_fixed_size: 101632
    .kernarg_segment_align: 8
    .kernarg_segment_size: 88
    .language:       OpenCL C
    .language_version:
      - 2
      - 0
    .max_flat_workgroup_size: 256
    .name:           _Z7k_graphPKfS0_S0_S0_S0_S0_S0_S0_S0_PfS1_
    .private_segment_fixed_size: 0
    .sgpr_count:     25
    .sgpr_spill_count: 0
    .symbol:         _Z7k_graphPKfS0_S0_S0_S0_S0_S0_S0_S0_PfS1_.kd
    .uniform_work_group_size: 1
    .uses_dynamic_stack: false
    .vgpr_count:     236
    .vgpr_spill_count: 0
    .wavefront_size: 64
  - .agpr_count:     0
    .args:
      - .actual_access:  read_only
        .address_space:  global
        .offset:         0
        .size:           8
        .value_kind:     global_buffer
      - .actual_access:  read_only
        .address_space:  global
        .offset:         8
        .size:           8
        .value_kind:     global_buffer
      - .actual_access:  read_only
        .address_space:  global
        .offset:         16
        .size:           8
        .value_kind:     global_buffer
      - .actual_access:  read_only
        .address_space:  global
        .offset:         24
        .size:           8
        .value_kind:     global_buffer
      - .actual_access:  read_only
        .address_space:  global
        .offset:         32
        .size:           8
        .value_kind:     global_buffer
      - .actual_access:  read_only
        .address_space:  global
        .offset:         40
        .size:           8
        .value_kind:     global_buffer
      - .actual_access:  read_only
        .address_space:  global
        .offset:         48
        .size:           8
        .value_kind:     global_buffer
      - .address_space:  global
        .offset:         56
        .size:           8
        .value_kind:     global_buffer
      - .actual_access:  read_only
        .address_space:  global
        .offset:         64
        .size:           8
        .value_kind:     global_buffer
      - .actual_access:  read_only
        .address_space:  global
        .offset:         72
        .size:           8
        .value_kind:     global_buffer
      - .actual_access:  read_only
        .address_space:  global
        .offset:         80
        .size:           8
        .value_kind:     global_buffer
      - .address_space:  global
        .offset:         88
        .size:           8
        .value_kind:     global_buffer
      - .actual_access:  write_only
        .address_space:  global
        .offset:         96
        .size:           8
        .value_kind:     global_buffer
      - .actual_access:  write_only
        .address_space:  global
        .offset:         104
        .size:           8
        .value_kind:     global_buffer
      - .actual_access:  write_only
        .address_space:  global
        .offset:         112
        .size:           8
        .value_kind:     global_buffer
      - .actual_access:  read_only
        .address_space:  global
        .offset:         120
        .size:           8
        .value_kind:     global_buffer
      - .actual_access:  read_only
        .address_space:  global
        .offset:         128
        .size:           8
        .value_kind:     global_buffer
      - .actual_access:  read_only
        .address_space:  global
        .offset:         136
        .size:           8
        .value_kind:     global_buffer
      - .actual_access:  read_only
        .address_space:  global
        .offset:         144
        .size:           8
        .value_kind:     global_buffer
      - .actual_access:  read_only
        .address_space:  global
        .offset:         152
        .size:           8
        .value_kind:     global_buffer
      - .actual_access:  read_only
        .address_space:  global
        .offset:         160
        .size:           8
        .value_kind:     global_buffer
      - .actual_access:  read_only
        .address_space:  global
        .offset:         168
        .size:           8
        .value_kind:     global_buffer
    .group_segment_fixed_size: 53792
    .kernarg_segment_align: 8
    .kernarg_segment_size: 176
    .language:       OpenCL C
    .language_version:
      - 2
      - 0
    .max_flat_workgroup_size: 512
    .name:           _Z9k_redprepILi1EEvPKfPKjS1_S1_S1_S1_S1_PfPKDv8_DF16_S7_S1_PDF16_S4_S4_S4_PKiS7_S1_S1_S1_S4_S4_
    .private_segment_fixed_size: 0
    .sgpr_count:     106
    .sgpr_spill_count: 4
    .symbol:         _Z9k_redprepILi1EEvPKfPKjS1_S1_S1_S1_S1_PfPKDv8_DF16_S7_S1_PDF16_S4_S4_S4_PKiS7_S1_S1_S1_S4_S4_.kd
    .uniform_work_group_size: 1
    .uses_dynamic_stack: false
    .vgpr_count:     104
    .vgpr_spill_count: 0
    .wavefront_size: 64
  - .agpr_count:     0
    .args:
      - .actual_access:  read_only
        .address_space:  global
        .offset:         0
        .size:           8
        .value_kind:     global_buffer
      - .actual_access:  read_only
        .address_space:  global
        .offset:         8
        .size:           8
        .value_kind:     global_buffer
      - .actual_access:  read_only
        .address_space:  global
        .offset:         16
        .size:           8
        .value_kind:     global_buffer
      - .actual_access:  read_only
        .address_space:  global
        .offset:         24
        .size:           8
        .value_kind:     global_buffer
      - .actual_access:  read_only
        .address_space:  global
        .offset:         32
        .size:           8
        .value_kind:     global_buffer
      - .actual_access:  read_only
        .address_space:  global
        .offset:         40
        .size:           8
        .value_kind:     global_buffer
      - .actual_access:  read_only
        .address_space:  global
        .offset:         48
        .size:           8
        .value_kind:     global_buffer
      - .address_space:  global
        .offset:         56
        .size:           8
        .value_kind:     global_buffer
      - .actual_access:  read_only
        .address_space:  global
        .offset:         64
        .size:           8
        .value_kind:     global_buffer
      - .actual_access:  read_only
        .address_space:  global
        .offset:         72
        .size:           8
        .value_kind:     global_buffer
      - .actual_access:  read_only
        .address_space:  global
        .offset:         80
        .size:           8
        .value_kind:     global_buffer
      - .actual_access:  read_only
        .address_space:  global
        .offset:         88
        .size:           8
        .value_kind:     global_buffer
      - .actual_access:  read_only
        .address_space:  global
        .offset:         96
        .size:           8
        .value_kind:     global_buffer
      - .actual_access:  read_only
        .address_space:  global
        .offset:         104
        .size:           8
        .value_kind:     global_buffer
      - .actual_access:  read_only
        .address_space:  global
        .offset:         112
        .size:           8
        .value_kind:     global_buffer
      - .actual_access:  read_only
        .address_space:  global
        .offset:         120
        .size:           8
        .value_kind:     global_buffer
      - .actual_access:  read_only
        .address_space:  global
        .offset:         128
        .size:           8
        .value_kind:     global_buffer
      - .actual_access:  read_only
        .address_space:  global
        .offset:         136
        .size:           8
        .value_kind:     global_buffer
      - .actual_access:  read_only
        .address_space:  global
        .offset:         144
        .size:           8
        .value_kind:     global_buffer
      - .actual_access:  read_only
        .address_space:  global
        .offset:         152
        .size:           8
        .value_kind:     global_buffer
      - .actual_access:  write_only
        .address_space:  global
        .offset:         160
        .size:           8
        .value_kind:     global_buffer
      - .address_space:  global
        .offset:         168
        .size:           8
        .value_kind:     global_buffer
    .group_segment_fixed_size: 66688
    .kernarg_segment_align: 8
    .kernarg_segment_size: 176
    .language:       OpenCL C
    .language_version:
      - 2
      - 0
    .max_flat_workgroup_size: 512
    .name:           _Z9k_redprepILi2EEvPKfPKjS1_S1_S1_S1_S1_PfPKDv8_DF16_S7_S1_PDF16_S4_S4_S4_PKiS7_S1_S1_S1_S4_S4_
    .private_segment_fixed_size: 0
    .sgpr_count:     104
    .sgpr_spill_count: 0
    .symbol:         _Z9k_redprepILi2EEvPKfPKjS1_S1_S1_S1_S1_PfPKDv8_DF16_S7_S1_PDF16_S4_S4_S4_PKiS7_S1_S1_S1_S4_S4_.kd
    .uniform_work_group_size: 1
    .uses_dynamic_stack: false
    .vgpr_count:     136
    .vgpr_spill_count: 0
    .wavefront_size: 64
